# strategy 4: one static s_setprio 1 for waves 4-7 across the attention loop (reset at the tail)
# baseline (speedup 1.0000x reference)
.LBB0_1343:
	s_and_b32 s3, s21, 3
	s_and_b64 s[4:5], exec, s[34:35]
	s_cselect_b32 s3, -1, s3
	s_cmp_eq_u32 s3, 2
	s_movk_i32 s4, 0x3080
	s_cselect_b32 s4, 0x2000, s4
	s_cmp_lg_u32 s3, 1
	s_cselect_b32 s4, s4, 0x1000
	s_cmp_gt_i32 s3, 0
	s_cselect_b32 s8, s4, 0
	s_mul_i32 s18, s8, 0xe00
	v_readlane_b32 s4, v253, 7
	v_readlane_b32 s5, v253, 8
	s_add_u32 s4, s4, s18
	v_lshlrev_b32_e32 v2, 8, v181
	v_mov_b32_e32 v3, v99
	v_lshl_add_u32 v7, v7, 7, v14
	s_addc_u32 s5, s5, 0
	v_lshlrev_b64 v[50:51], 1, v[2:3]
	v_cvt_pk_bf16_f32 v5, v5, v99
	ds_write_b16 v7, v5
	v_cvt_pk_bf16_f32 v4, v4, v99
	v_lshl_add_u64 v[2:3], s[4:5], 0, v[50:51]
	ds_write_b16 v7, v4 offset:32
	v_ashrrev_i32_e32 v4, 4, v6
	v_lshlrev_b32_e32 v5, 3, v6
	s_movk_i32 s4, 0x700
	v_and_b32_e32 v7, 0x78, v5
	v_mul_lo_u32 v8, v4, s4
	v_or_b32_e32 v8, v8, v7
	v_lshlrev_b32_e32 v52, 1, v8
	v_readfirstlane_b32 s4, v2
	v_readfirstlane_b32 s5, v3
	s_waitcnt lgkmcnt(0)
	s_barrier
	v_add_u32_e32 v54, 0x1c000, v52
	s_nop 1
	global_load_dwordx4 v[8:11], v52, s[4:5] offset:1792
	global_load_dwordx4 v[14:17], v54, s[4:5] offset:1792
	s_lshl_b32 s22, s8, 7
	v_readlane_b32 s8, v253, 5
	v_lshlrev_b32_e32 v26, 4, v6
	v_readlane_b32 s9, v253, 6
	s_add_u32 s24, s8, s22
	v_ashrrev_i32_e32 v13, 3, v6
	v_and_b32_e32 v30, 0x70, v26
	s_addc_u32 s25, s9, 0
	v_lshl_or_b32 v56, v13, 7, v30
	global_load_dwordx4 v[18:21], v52, s[4:5] offset:1536
	global_load_dwordx4 v[22:25], v54, s[4:5] offset:1536
	global_load_dwordx4 v[26:29], v56, s[24:25]
	v_lshlrev_b32_e32 v31, 7, v194
	v_lshlrev_b32_e32 v12, 1, v12
	v_readlane_b32 s4, v255, 34
	v_lshlrev_b32_e32 v32, 1, v4
	v_lshrrev_b32_e32 v33, 1, v4
	v_add3_u32 v12, s4, v31, v12
	v_and_b32_e32 v31, 0xfffff0, v4
	v_and_b32_e32 v35, 3, v4
	v_add_u32_e32 v36, 32, v4
	s_add_i32 s4, 0, 0x14000
	ds_read_b128 v[144:147], v12
	ds_read_b128 v[140:143], v12 offset:32
	ds_read_b128 v[136:139], v12 offset:64
	ds_read_b128 v[132:135], v12 offset:96
	v_and_or_b32 v12, v32, 8, v31
	v_and_or_b32 v31, v33, 4, v35
	v_and_b32_e32 v32, 0xfffff0, v36
	v_lshlrev_b32_e32 v33, 1, v36
	s_and_b64 s[0:1], s[0:1], exec
	v_bfe_u32 v34, v5, 5, 2
	v_lshrrev_b32_e32 v12, 1, v12
	v_and_or_b32 v32, v33, 8, v32
	s_cselect_b32 s5, 0x104, 4
	s_cmp_lt_u32 s3, 2
	v_lshlrev_b32_e32 v7, 1, v7
	v_or_b32_e32 v12, v12, v34
	v_lshrrev_b32_e32 v32, 1, v32
	s_cselect_b32 s3, 64, 0x42
	s_and_b64 s[0:1], exec, s[34:35]
	v_lshlrev_b32_e32 v31, 6, v31
	v_and_b32_e32 v35, 48, v7
	v_lshlrev_b32_e32 v12, 9, v12
	v_or_b32_e32 v32, v32, v34
	s_cselect_b32 s3, s5, s3
	s_add_i32 s0, 0, 0x8000
	v_lshlrev_b32_e32 v32, 9, v32
	v_or3_b32 v12, v12, v31, v35
	s_cmp_lg_u32 s0, -1
	v_or3_b32 v31, v32, v31, v35
	v_add_u32_e32 v205, 0, v12
	s_cselect_b32 s0, s0, 0
	s_movk_i32 s8, 0x70
	v_add_u32_e32 v206, 0, v31
	s_waitcnt vmcnt(0)
	v_mov_b32_e32 v12, s0
	s_movk_i32 s0, 0x180
	v_mul_lo_u32 v4, v4, s0
	v_bitop3_b32 v37, v98, v5, s8 bitop3:0x78
	s_waitcnt vmcnt(4)
	ds_write_b128 v205, v[8:11]
	s_waitcnt vmcnt(3)
	ds_write_b128 v206, v[14:17]
	v_lshrrev_b32_e32 v8, 1, v6
	v_bitop3_b32 v7, v7, v8, s8 bitop3:0x78
	v_add3_u32 v207, v7, v4, 0
	v_mul_lo_u32 v4, v13, s0
	v_or_b32_e32 v7, 0x100, v30
	v_and_b32_e32 v8, 0x70, v6
	v_mad_u32_u24 v53, v195, s0, v12
	v_xad_u32 v4, v7, v8, v4
	v_add_u32_e32 v201, v37, v53
	v_add_u32_e32 v208, 0, v4
	s_waitcnt vmcnt(2)
	ds_write_b128 v207, v[18:21] offset:32768
	s_waitcnt vmcnt(1)
	ds_write_b128 v207, v[22:25] offset:45056
	s_waitcnt vmcnt(0)
	ds_write_b128 v208, v[26:29] offset:32768
	s_waitcnt lgkmcnt(0)
	s_barrier
	ds_read_b128 v[8:11], v201
	ds_read_b128 v[12:15], v201 offset:128
	s_waitcnt lgkmcnt(1)
	v_mfma_f32_32x32x16_bf16 v[18:33], v[8:11], v[128:131], 0
	ds_read_b128 v[8:11], v201 offset:12288
	ds_read_b128 v[60:63], v201 offset:256
	v_and_b32_e32 v4, 0x70, v5
	v_bitop3_b32 v5, v98, v4, 32 bitop3:0x36
	v_add_u32_e32 v203, v5, v53
	v_bitop3_b32 v5, v98, v4, 64 bitop3:0x36
	v_add_u32_e32 v204, v5, v53
	s_waitcnt lgkmcnt(1)
	v_mfma_f32_32x32x16_bf16 v[34:49], v[8:11], v[128:131], 0
	ds_read_b128 v[8:11], v203
	ds_read_b128 v[64:67], v203 offset:128
	ds_read_b128 v[68:71], v203 offset:256
	s_movk_i32 s0, 0x60
	v_bitop3_b32 v4, v98, v4, s0 bitop3:0x36
	v_add_u32_e32 v202, v4, v53
	s_mov_b64 s[0:1], 0x38700
	v_lshl_add_u64 v[4:5], v[2:3], 0, s[0:1]
	s_waitcnt lgkmcnt(2)
	v_mfma_f32_32x32x16_bf16 v[18:33], v[8:11], v[124:127], v[18:33]
	ds_read_b128 v[8:11], v203 offset:12288
	s_mov_b64 s[0:1], 0x38600
	v_lshl_add_u64 v[2:3], v[2:3], 0, s[0:1]
	v_readfirstlane_b32 s0, v4
	v_readfirstlane_b32 s1, v5
	v_readfirstlane_b32 s8, v2
	v_readfirstlane_b32 s9, v3
	s_waitcnt lgkmcnt(0)
	v_mfma_f32_32x32x16_bf16 v[34:49], v[8:11], v[124:127], v[34:49]
	ds_read_b128 v[8:11], v204
	ds_read_b128 v[72:75], v204 offset:128
	ds_read_b128 v[76:79], v204 offset:256
	v_mov_b32_e32 v57, v99
	v_add_u32_e32 v209, 0x3000, v207
	s_cmp_lg_u32 0, -1
	v_lshlrev_b32_e32 v4, 1, v58
	v_and_b32_e32 v4, 32, v4
	s_waitcnt lgkmcnt(2)
	v_mfma_f32_32x32x16_bf16 v[18:33], v[8:11], v[120:123], v[18:33]
	ds_read_b128 v[8:11], v204 offset:12288
	s_mov_b32 s36, s63
	s_mov_b32 s37, s63
	s_mov_b32 s19, s63
	s_mov_b32 s38, s63
	s_mov_b32 s39, s63
	s_mov_b32 s40, s63
	s_waitcnt lgkmcnt(0)
	v_mfma_f32_32x32x16_bf16 v[34:49], v[8:11], v[120:123], v[34:49]
	ds_read_b128 v[8:11], v202
	ds_read_b128 v[80:83], v202 offset:128
	s_mov_b32 s41, s63
	s_mov_b32 s42, s63
	s_mov_b32 s43, s63
	s_mov_b32 s44, s63
	s_mov_b32 s45, s63
	s_mov_b32 s46, s63
	s_waitcnt lgkmcnt(1)
	v_mfma_f32_32x32x16_bf16 v[18:33], v[8:11], v[116:119], v[18:33]
	ds_read_b128 v[8:11], v202 offset:12288
	ds_read_b128 v[84:87], v202 offset:256
	s_mov_b32 s47, s63
	s_mov_b32 s48, s63
	s_mov_b32 s49, s63
	s_mov_b32 s50, s63
	s_mov_b32 s51, s63
	s_mov_b32 s23, s63
	v_mfma_f32_32x32x16_bf16 v[18:33], v[12:15], v[112:115], v[18:33]
	v_mov_b32_e32 v53, v99
	v_mov_b32_e32 v55, v99
	v_lshl_add_u64 v[182:183], s[22:23], 0, v[56:57]
	v_mov_b32_e32 v227, 0x3200
	v_mov_b32_e32 v199, 0
	s_waitcnt lgkmcnt(1)
	v_mfma_f32_32x32x16_bf16 v[34:49], v[8:11], v[116:119], v[34:49]
	ds_read_b128 v[8:11], v201 offset:12416
	ds_read_b128 v[12:15], v201 offset:12544
	v_mfma_f32_32x32x16_bf16 v[18:33], v[64:67], v[108:111], v[18:33]
	s_waitcnt lgkmcnt(1)
	v_mfma_f32_32x32x16_bf16 v[34:49], v[8:11], v[112:115], v[34:49]
	ds_read_b128 v[8:11], v203 offset:12416
	ds_read_b128 v[64:67], v203 offset:12544
	v_mfma_f32_32x32x16_bf16 v[18:33], v[72:75], v[104:107], v[18:33]
	s_waitcnt lgkmcnt(1)
	v_mfma_f32_32x32x16_bf16 v[34:49], v[8:11], v[108:111], v[34:49]
	ds_read_b128 v[8:11], v204 offset:12416
	ds_read_b128 v[72:75], v204 offset:12544
	v_mfma_f32_32x32x16_bf16 v[18:33], v[80:83], v[100:103], v[18:33]
	s_waitcnt lgkmcnt(1)
	v_mfma_f32_32x32x16_bf16 v[34:49], v[8:11], v[104:107], v[34:49]
	ds_read_b128 v[8:11], v202 offset:12416
	ds_read_b128 v[80:83], v202 offset:12544
	v_mfma_f32_32x32x16_bf16 v[18:33], v[60:63], v[144:147], v[18:33]
	global_load_dwordx4 v[60:63], v54, s[0:1]
	global_load_dwordx4 v[88:91], v52, s[8:9]
	global_load_dwordx4 v[92:95], v52, s[0:1]
	global_load_dwordx4 v[148:151], v54, s[8:9]
	s_movk_i32 s0, 0x2000
	s_mov_b32 s8, 2
	s_waitcnt lgkmcnt(1)
	v_mfma_f32_32x32x16_bf16 v[34:49], v[8:11], v[100:103], v[34:49]
	v_lshl_add_u64 v[8:9], s[24:25], 0, v[56:57]
	v_add_co_u32_e32 v2, vcc, s0, v8
	v_cmp_gt_u32_e64 s[0:1], 32, v58
	s_nop 0
	v_addc_co_u32_e32 v3, vcc, 0, v9, vcc
	global_load_dwordx4 v[152:155], v[2:3], off
	v_mfma_f32_32x32x16_bf16 v[18:33], v[68:71], v[140:143], v[18:33]
	s_waitcnt vmcnt(0)
	s_waitcnt vmcnt(2)
	ds_write_b128 v205, v[92:95] offset:16384
	ds_write_b128 v206, v[60:63] offset:16384
	ds_write_b128 v207, v[88:91] offset:57344
	s_waitcnt vmcnt(1)
	ds_write_b128 v209, v[148:151] offset:57344
	s_waitcnt vmcnt(0)
	ds_write_b128 v208, v[152:155] offset:57344
	v_mfma_f32_32x32x16_bf16 v[34:49], v[12:15], v[144:147], v[34:49]
	v_and_b32_e32 v2, 0x3fffffc0, v6
	v_lshl_add_u32 v196, v2, 2, s4
	s_cselect_b32 s4, 0, 0
	v_lshlrev_b32_e32 v3, 4, v58
	v_lshlrev_b32_e32 v2, 3, v58
	v_and_b32_e32 v3, 0xc0, v3
	v_and_or_b32 v3, v2, 24, v3
	v_mfma_f32_32x32x16_bf16 v[18:33], v[76:79], v[136:139], v[18:33]
	v_and_b32_e32 v2, 0x100, v2
	v_or3_b32 v59, v3, v4, v2
	v_mov_b64_e32 v[2:3], s[36:37]
	v_add_u32_e32 v200, s4, v59
	v_mov_b64_e32 v[16:17], s[50:51]
	v_mov_b64_e32 v[4:5], s[38:39]
	v_mov_b64_e32 v[6:7], s[40:41]
	v_mfma_f32_32x32x16_bf16 v[34:49], v[64:67], v[140:143], v[34:49]
	v_mov_b64_e32 v[8:9], s[42:43]
	v_mov_b64_e32 v[10:11], s[44:45]
	v_mov_b64_e32 v[12:13], s[46:47]
	v_mov_b64_e32 v[14:15], s[48:49]
	v_lshl_add_u32 v197, v195, 2, v196
	s_waitcnt lgkmcnt(0)
	s_barrier
	v_mfma_f32_32x32x16_bf16 v[18:33], v[84:87], v[132:135], v[18:33]
	v_mfma_f32_32x32x16_bf16 v[34:49], v[72:75], v[136:139], v[34:49]
	s_nop 10
	v_max_f32_e32 v64, v19, v19
	v_max_f32_e32 v65, v18, v18
	v_max_f32_e32 v64, v65, v64
	v_max3_f32 v64, v64, v20, v21
	v_max3_f32 v64, v64, v22, v23
	v_max3_f32 v64, v64, v24, v25
	v_max3_f32 v64, v64, v26, v27
	v_mfma_f32_32x32x16_bf16 v[34:49], v[80:83], v[132:135], v[34:49]
	v_max3_f32 v64, v64, v28, v29
	v_max3_f32 v64, v64, v30, v31
	v_max3_f32 v64, v64, v32, v33
	s_nop 8
	v_max3_f32 v64, v64, v34, v35
	v_max3_f32 v64, v64, v36, v37
	v_max3_f32 v64, v64, v38, v39
	v_max3_f32 v64, v64, v40, v41
	v_max3_f32 v64, v64, v42, v43
	v_max3_f32 v64, v64, v44, v45
	v_max3_f32 v64, v64, v46, v47
	v_max3_f32 v64, v64, v48, v49
	v_mov_b32_e32 v65, v64
	s_nop 1
	v_permlane32_swap_b32_e32 v64, v65
	v_max_f32_e32 v65, v65, v65
	v_max_f32_e32 v64, v64, v64
	v_max_f32_e32 v64, v64, v65
	v_max_f32_e32 v60, 0xf149f2ca, v64
	v_sub_f32_e32 v61, 0xf149f2ca, v60
	v_mul_f32_e32 v61, 0x3dd53b94, v61
	v_add_f32_e32 v65, 0x7149f2ca, v64
	v_exp_f32_e32 v61, v61
	v_cmp_ge_f32_e32 vcc, s11, v65
	s_cmp_eq_u64 vcc, exec
	s_cselect_b64 vcc, -1, 0
	v_cndmask_b32_e64 v210, v61, 1.0, vcc
	v_mov_b32_e32 v61, 0xf149f2ca
	v_cndmask_b32_e32 v211, v60, v61, vcc
	v_mul_f32_e32 v60, 0xbdd53b94, v211
	v_fmamk_f32 v18, v18, 0x3dd53b94, v60
	v_exp_f32_e32 v169, v18
	v_fmamk_f32 v18, v19, 0x3dd53b94, v60
	v_exp_f32_e32 v191, v18
	v_fmamk_f32 v18, v20, 0x3dd53b94, v60
	v_exp_f32_e32 v170, v18
	v_fmamk_f32 v18, v21, 0x3dd53b94, v60
	v_exp_f32_e32 v192, v18
	v_fmamk_f32 v18, v22, 0x3dd53b94, v60
	v_exp_f32_e32 v190, v18
	v_fmamk_f32 v18, v23, 0x3dd53b94, v60
	v_exp_f32_e32 v193, v18
	v_fmamk_f32 v18, v24, 0x3dd53b94, v60
	v_exp_f32_e32 v171, v18
	v_fmamk_f32 v18, v25, 0x3dd53b94, v60
	v_exp_f32_e32 v189, v18
	v_fmamk_f32 v18, v26, 0x3dd53b94, v60
	v_exp_f32_e32 v173, v18
	v_fmamk_f32 v18, v27, 0x3dd53b94, v60
	v_exp_f32_e32 v175, v18
	v_fmamk_f32 v18, v28, 0x3dd53b94, v60
	v_exp_f32_e32 v174, v18
	v_fmamk_f32 v18, v29, 0x3dd53b94, v60
	v_exp_f32_e32 v188, v18
	v_fmamk_f32 v18, v30, 0x3dd53b94, v60
	v_exp_f32_e32 v164, v18
	v_fmamk_f32 v18, v31, 0x3dd53b94, v60
	v_pk_fma_f32 v[148:149], v[48:49], s[56:57], v[60:61] op_sel_hi:[1,0,0]
	v_pk_fma_f32 v[154:155], v[46:47], s[56:57], v[60:61] op_sel_hi:[1,0,0]
	v_pk_fma_f32 v[158:159], v[44:45], s[56:57], v[60:61] op_sel_hi:[1,0,0]
	v_pk_fma_f32 v[150:151], v[42:43], s[56:57], v[60:61] op_sel_hi:[1,0,0]
	v_pk_fma_f32 v[152:153], v[40:41], s[56:57], v[60:61] op_sel_hi:[1,0,0]
	v_pk_fma_f32 v[156:157], v[38:39], s[56:57], v[60:61] op_sel_hi:[1,0,0]
	v_pk_fma_f32 v[160:161], v[36:37], s[56:57], v[60:61] op_sel_hi:[1,0,0]
	v_pk_fma_f32 v[162:163], v[34:35], s[56:57], v[60:61] op_sel_hi:[1,0,0]
	v_exp_f32_e32 v166, v18
	v_fmamk_f32 v18, v32, 0x3dd53b94, v60
	v_fmac_f32_e32 v60, 0x3dd53b94, v33
	v_exp_f32_e32 v165, v18
	v_exp_f32_e32 v167, v60
	s_addk_i32 s4, 0x4000
	v_lshl_add_u64 v[18:19], s[18:19], 0, v[50:51]
	v_add_u32_e32 v198, s4, v59
	v_lshl_add_u64 v[184:185], v[18:19], 0, v[54:55]
	v_lshl_add_u64 v[186:187], v[18:19], 0, v[52:53]
	v_mov_b64_e32 v[64:65], v[16:17]
	v_mov_b64_e32 v[48:49], v[16:17]
	v_mov_b64_e32 v[32:33], v[16:17]
	v_mov_b64_e32 v[62:63], v[14:15]
	v_mov_b64_e32 v[60:61], v[12:13]
	v_mov_b64_e32 v[58:59], v[10:11]
	v_mov_b64_e32 v[56:57], v[8:9]
	v_mov_b64_e32 v[54:55], v[6:7]
	v_mov_b64_e32 v[52:53], v[4:5]
	v_mov_b64_e32 v[50:51], v[2:3]
	v_mov_b64_e32 v[46:47], v[14:15]
	v_mov_b64_e32 v[44:45], v[12:13]
	v_mov_b64_e32 v[42:43], v[10:11]
	v_mov_b64_e32 v[40:41], v[8:9]
	v_mov_b64_e32 v[38:39], v[6:7]
	v_mov_b64_e32 v[36:37], v[4:5]
	v_mov_b64_e32 v[34:35], v[2:3]
	v_mov_b64_e32 v[30:31], v[14:15]
	v_mov_b64_e32 v[28:29], v[12:13]
	v_mov_b64_e32 v[26:27], v[10:11]
	v_mov_b64_e32 v[24:25], v[8:9]
	v_mov_b64_e32 v[22:23], v[6:7]
	v_mov_b64_e32 v[20:21], v[4:5]
	v_mov_b64_e32 v[18:19], v[2:3]
	v_and_b32_e32 v230, 63, v0
	v_lshrrev_b32_e32 v231, 6, v0
	v_lshrrev_b32_e32 v232, 4, v0
	v_mul_u32_u24_e32 v232, 0xe00, v232
	v_and_b32_e32 v233, 15, v0
	v_lshl_add_u32 v232, v233, 4, v232
	v_sub_u32_e32 v232, v186, v232
	v_lshrrev_b32_e32 v233, 3, v0
	v_and_b32_e32 v236, 7, v0
	v_lshlrev_b32_e32 v236, 4, v236
	v_lshl_add_u32 v233, v233, 7, v236
	v_sub_u32_e32 v233, v182, v233
	v_add_u32_e32 v232, 0x39d1dc00, v232
	v_add_u32_e32 v233, 0x39b15600, v233
	v_mov_b32_e32 v243, 0
	v_mov_b32_e32 v244, 0x2000
	v_mov_b32_e32 v245, 0x38000
	v_bfe_u32 v236, v230, 2, 3
	v_lshl_add_u32 v236, v231, 3, v236
	v_and_b32_e32 v237, 0xfffffff3, v236
	v_and_b32_e32 v238, 4, v236
	v_lshl_or_b32 v237, v238, 1, v237
	v_and_b32_e32 v238, 8, v236
	v_lshrrev_b32_e32 v238, 1, v238
	v_or_b32_e32 v237, v237, v238
	v_add_u32_e32 v237, 64, v237
	v_mul_u32_u24_e32 v237, 0xe00, v237
	v_add_u32_e32 v237, v237, v232
	v_lshrrev_b32_e32 v238, 5, v230
	v_lshlrev_b32_e32 v238, 6, v238
	v_and_b32_e32 v239, 3, v230
	v_lshl_add_u32 v238, v239, 4, v238
	v_add_u32_e32 v237, v237, v238
	v_add_u32_e32 v242, 0x100, v237
	v_lshl_add_u64 v[206:207], s[14:15], 0, v[242:243]
	v_mov_b32_e32 v236, v230
	v_mul_u32_u24_e32 v237, 0x2ab, v236
	v_lshrrev_b32_e32 v237, 14, v237
	v_mul_u32_u24_e32 v238, 24, v237
	v_sub_u32_e32 v238, v236, v238
	v_lshl_add_u32 v237, v231, 3, v237
	v_bfe_u32 v239, v237, 1, 3
	v_xor_b32_e32 v238, v238, v239
	v_add_u32_e32 v237, 0x80, v237
	v_mul_u32_u24_e32 v240, 0xe00, v237
	v_add_u32_e32 v240, v240, v232
	v_lshl_add_u32 v240, v238, 4, v240
	v_lshl_add_u32 v241, v237, 7, v233
	v_lshl_add_u32 v241, v238, 4, v241
	v_subrev_u32_e32 v241, 0x100, v241
	v_cmp_gt_u32_e32 vcc, 16, v238
	s_nop 1
	v_cndmask_b32_e32 v242, v241, v240, vcc
	v_cndmask_b32_e32 v205, v244, v245, vcc
	v_lshl_add_u64 v[182:183], s[14:15], 0, v[242:243]
	v_add_u32_e32 v236, 0x40, v230
	v_mul_u32_u24_e32 v237, 0x2ab, v236
	v_lshrrev_b32_e32 v237, 14, v237
	v_mul_u32_u24_e32 v238, 24, v237
	v_sub_u32_e32 v238, v236, v238
	v_lshl_add_u32 v237, v231, 3, v237
	v_bfe_u32 v239, v237, 1, 3
	v_xor_b32_e32 v238, v238, v239
	v_add_u32_e32 v237, 0x80, v237
	v_mul_u32_u24_e32 v240, 0xe00, v237
	v_add_u32_e32 v240, v240, v232
	v_lshl_add_u32 v240, v238, 4, v240
	v_lshl_add_u32 v241, v237, 7, v233
	v_lshl_add_u32 v241, v238, 4, v241
	v_subrev_u32_e32 v241, 0x100, v241
	v_cmp_gt_u32_e32 vcc, 16, v238
	s_nop 1
	v_cndmask_b32_e32 v242, v241, v240, vcc
	v_cndmask_b32_e32 v208, v244, v245, vcc
	v_lshl_add_u64 v[184:185], s[14:15], 0, v[242:243]
	v_add_u32_e32 v236, 0x80, v230
	v_mul_u32_u24_e32 v237, 0x2ab, v236
	v_lshrrev_b32_e32 v237, 14, v237
	v_mul_u32_u24_e32 v238, 24, v237
	v_sub_u32_e32 v238, v236, v238
	v_lshl_add_u32 v237, v231, 3, v237
	v_bfe_u32 v239, v237, 1, 3
	v_xor_b32_e32 v238, v238, v239
	v_add_u32_e32 v237, 0x80, v237
	v_mul_u32_u24_e32 v240, 0xe00, v237
	v_add_u32_e32 v240, v240, v232
	v_lshl_add_u32 v240, v238, 4, v240
	v_lshl_add_u32 v241, v237, 7, v233
	v_lshl_add_u32 v241, v238, 4, v241
	v_subrev_u32_e32 v241, 0x100, v241
	v_cmp_gt_u32_e32 vcc, 16, v238
	s_nop 1
	v_cndmask_b32_e32 v242, v241, v240, vcc
	v_cndmask_b32_e32 v209, v244, v245, vcc
	v_lshl_add_u64 v[186:187], s[14:15], 0, v[242:243]
	v_readfirstlane_b32 s98, v0
	s_nop 3
	s_lshr_b32 s98, s98, 8
	s_cmp_lg_u32 s98, 0
	s_cbranch_scc0 .Latt_prio_done
	s_setprio 1
.Latt_prio_done:
.LBB0_1344:
	ds_read_b128 v[230:233], v203 offset:24576
	ds_read_b128 v[236:239], v203 offset:36864
	ds_read_b128 v[240:243], v204 offset:24576
	ds_read_b128 v[244:247], v204 offset:36864
	ds_read_b128 v[66:69], v201 offset:36864
	ds_read_b128 v[70:73], v201 offset:24576
	ds_read_b128 v[212:215], v202 offset:24576
	ds_read_b128 v[216:219], v202 offset:36864
	v_add_f32_e32 v168, 0, v169
	v_add_f32_e32 v168, v191, v168
	v_add_f32_e32 v168, v170, v168
	s_waitcnt lgkmcnt(2)
	v_mfma_f32_32x32x16_bf16 v[82:97], v[70:73], v[128:131], 0
	v_add_f32_e32 v168, v192, v168
	v_add_f32_e32 v168, v190, v168
	v_add_f32_e32 v168, v193, v168
	v_add_f32_e32 v168, v171, v168
	v_add_f32_e32 v168, v189, v168
	v_add_f32_e32 v168, v173, v168
	v_add_f32_e32 v168, v175, v168
	v_mfma_f32_32x32x16_bf16 v[66:81], v[66:69], v[128:131], 0
	v_add_f32_e32 v168, v174, v168
	v_add_f32_e32 v168, v188, v168
	v_exp_f32_e32 v162, v162
	v_add_f32_e32 v168, v164, v168
	v_exp_f32_e32 v163, v163
	v_add_f32_e32 v168, v166, v168
	v_exp_f32_e32 v160, v160
	v_mfma_f32_32x32x16_bf16 v[82:97], v[230:233], v[124:127], v[82:97]
	v_add_f32_e32 v168, v165, v168
	v_exp_f32_e32 v161, v161
	v_add_f32_e32 v168, v167, v168
	v_exp_f32_e32 v156, v156
	v_add_f32_e32 v168, v162, v168
	v_exp_f32_e32 v157, v157
	v_add_f32_e32 v168, v163, v168
	v_mfma_f32_32x32x16_bf16 v[66:81], v[236:239], v[124:127], v[66:81]
	ds_read_b128 v[230:233], v201 offset:24704
	ds_read_b128 v[236:239], v201 offset:36992
	v_exp_f32_e32 v152, v152
	v_add_f32_e32 v168, v160, v168
	v_exp_f32_e32 v153, v153
	v_add_f32_e32 v168, v161, v168
	v_exp_f32_e32 v150, v150
	v_add_f32_e32 v168, v156, v168
	v_mfma_f32_32x32x16_bf16 v[82:97], v[240:243], v[120:123], v[82:97]
	v_exp_f32_e32 v151, v151
	v_add_f32_e32 v168, v157, v168
	v_exp_f32_e32 v158, v158
	v_add_f32_e32 v168, v152, v168
	v_exp_f32_e32 v159, v159
	v_add_f32_e32 v168, v153, v168
	v_exp_f32_e32 v154, v154
	v_mfma_f32_32x32x16_bf16 v[66:81], v[244:247], v[120:123], v[66:81]
	ds_read_b128 v[240:243], v203 offset:24704
	ds_read_b128 v[244:247], v203 offset:36992
	v_add_f32_e32 v168, v150, v168
	v_exp_f32_e32 v155, v155
	v_add_f32_e32 v168, v151, v168
	v_exp_f32_e32 v148, v148
	v_add_f32_e32 v168, v158, v168
	v_exp_f32_e32 v149, v149
	s_waitcnt lgkmcnt(5)
	v_mfma_f32_32x32x16_bf16 v[82:97], v[212:215], v[116:119], v[82:97]
	v_add_f32_e32 v168, v159, v168
	v_add_f32_e32 v168, v154, v168
	v_add_f32_e32 v168, v155, v168
	v_add_f32_e32 v168, v148, v168
	s_waitcnt lgkmcnt(4)
	v_mfma_f32_32x32x16_bf16 v[66:81], v[216:219], v[116:119], v[66:81]
	ds_read_b128 v[212:215], v204 offset:24704
	ds_read_b128 v[216:219], v204 offset:36992
	s_waitcnt lgkmcnt(5)
	v_mfma_f32_32x32x16_bf16 v[82:97], v[230:233], v[112:115], v[82:97]
	s_waitcnt lgkmcnt(4)
	v_mfma_f32_32x32x16_bf16 v[66:81], v[236:239], v[112:115], v[66:81]
	ds_read_b128 v[230:233], v202 offset:24704
	ds_read_b128 v[236:239], v202 offset:36992
	s_waitcnt lgkmcnt(5)
	v_mfma_f32_32x32x16_bf16 v[82:97], v[240:243], v[108:111], v[82:97]
	s_waitcnt lgkmcnt(4)
	v_mfma_f32_32x32x16_bf16 v[66:81], v[244:247], v[108:111], v[66:81]
	ds_read_b128 v[240:243], v201 offset:24832
	ds_read_b128 v[244:247], v201 offset:37120
	s_waitcnt lgkmcnt(5)
	v_mfma_f32_32x32x16_bf16 v[82:97], v[212:215], v[104:107], v[82:97]
	s_waitcnt lgkmcnt(4)
	v_mfma_f32_32x32x16_bf16 v[66:81], v[216:219], v[104:107], v[66:81]
	ds_read_b128 v[212:215], v203 offset:24832
	ds_read_b128 v[216:219], v203 offset:37120
	s_waitcnt lgkmcnt(5)
	v_mfma_f32_32x32x16_bf16 v[82:97], v[230:233], v[100:103], v[82:97]
	s_waitcnt lgkmcnt(4)
	v_mfma_f32_32x32x16_bf16 v[66:81], v[236:239], v[100:103], v[66:81]
	ds_read_b128 v[230:233], v204 offset:24832
	ds_read_b128 v[236:239], v204 offset:37120
	s_waitcnt lgkmcnt(5)
	v_mfma_f32_32x32x16_bf16 v[82:97], v[240:243], v[144:147], v[82:97]
	s_waitcnt lgkmcnt(4)
	v_mfma_f32_32x32x16_bf16 v[66:81], v[244:247], v[144:147], v[66:81]
	ds_read_b128 v[240:243], v202 offset:24832
	ds_read_b128 v[244:247], v202 offset:37120
	s_waitcnt lgkmcnt(5)
	v_mfma_f32_32x32x16_bf16 v[82:97], v[212:215], v[140:143], v[82:97]
	v_add_f32_e32 v212, v149, v168
	v_mov_b32_e32 v213, v212
	v_cvt_pk_bf16_f32 v168, v169, v191
	v_cvt_pk_bf16_f32 v169, v170, v192
	v_cvt_pk_bf16_f32 v170, v190, v193
	v_cvt_pk_bf16_f32 v171, v171, v189
	v_cvt_pk_bf16_f32 v172, v173, v175
	s_waitcnt lgkmcnt(4)
	v_mfma_f32_32x32x16_bf16 v[66:81], v[216:219], v[140:143], v[66:81]
	v_cvt_pk_bf16_f32 v173, v174, v188
	v_cvt_pk_bf16_f32 v174, v164, v166
	v_permlane32_swap_b32_e32 v212, v213
	v_permlane32_swap_b32_e32 v168, v170
	v_cvt_pk_bf16_f32 v175, v165, v167
	s_waitcnt lgkmcnt(3)
	v_mfma_f32_32x32x16_bf16 v[82:97], v[230:233], v[136:139], v[82:97]
	v_permlane32_swap_b32_e32 v172, v174
	v_cvt_pk_bf16_f32 v214, v162, v163
	v_cvt_pk_bf16_f32 v215, v160, v161
	v_cvt_pk_bf16_f32 v216, v156, v157
	v_cvt_pk_bf16_f32 v217, v152, v153
	v_cvt_pk_bf16_f32 v230, v150, v151
	s_waitcnt lgkmcnt(2)
	v_mfma_f32_32x32x16_bf16 v[66:81], v[236:239], v[136:139], v[66:81]
	v_cvt_pk_bf16_f32 v231, v158, v159
	v_cvt_pk_bf16_f32 v232, v154, v155
	v_cvt_pk_bf16_f32 v233, v148, v149
	v_permlane32_swap_b32_e32 v169, v171
	v_permlane32_swap_b32_e32 v173, v175
	s_waitcnt lgkmcnt(1)
	v_mfma_f32_32x32x16_bf16 v[82:97], v[240:243], v[132:135], v[82:97]
	v_permlane32_swap_b32_e32 v214, v216
	v_permlane32_swap_b32_e32 v215, v217
	v_permlane32_swap_b32_e32 v230, v232
	v_permlane32_swap_b32_e32 v231, v233
	s_waitcnt lgkmcnt(0)
	v_mfma_f32_32x32x16_bf16 v[66:81], v[244:247], v[132:135], v[66:81]
	v_readfirstlane_b32 s4, v0
	s_nop 0
	s_lshl_b32 s5, s4, 4
	s_mul_i32 s4, s5, 3
	s_add_i32 m0, s4, 0x8000
	s_nop 0
	global_load_lds_dwordx4 v[182:183], off
	s_add_i32 m0, s4, 0x8400
	s_nop 0
	global_load_lds_dwordx4 v[184:185], off
	s_add_i32 m0, s4, 0x8800
	s_nop 0
	global_load_lds_dwordx4 v[186:187], off
	s_lshl_b32 s5, s5, 1
	s_add_i32 m0, s5, 0x4000
	s_nop 0
	global_load_lds_dwordx4 v[206:207], off
	s_add_i32 m0, s5, 0x4380
	s_nop 0
	global_load_lds_dwordx4 v[206:207], off offset:128
	v_add_co_u32_e32 v182, vcc, v182, v205
	s_nop 1
	v_addc_co_u32_e32 v183, vcc, 0, v183, vcc
	v_add_co_u32_e32 v184, vcc, v184, v208
	s_nop 1
	v_addc_co_u32_e32 v185, vcc, 0, v185, vcc
	v_add_co_u32_e32 v186, vcc, v186, v209
	s_nop 1
	v_addc_co_u32_e32 v187, vcc, 0, v187, vcc
	v_add_co_u32_e32 v206, vcc, 0x38000, v206
	s_nop 1
	v_addc_co_u32_e32 v207, vcc, 0, v207, vcc
	ds_read_b64_tr_b16 v[236:237], v200 offset:0
	ds_read_b64_tr_b16 v[238:239], v200 offset:0x800
	ds_read_b64_tr_b16 v[240:241], v200 offset:0x1000
	ds_read_b64_tr_b16 v[242:243], v200 offset:0x1800
	ds_read_b64_tr_b16 v[244:245], v200 offset:0x2000
	ds_read_b64_tr_b16 v[246:247], v200 offset:0x2800
	ds_read_b64_tr_b16 v[222:223], v200 offset:0x3000
	ds_read_b64_tr_b16 v[224:225], v200 offset:0x3800
	s_waitcnt lgkmcnt(0)
	s_nop 0
	v_mfma_f32_32x32x16_bf16 v[2:17], v[168:171], v[236:239], v[2:17]
	v_mfma_f32_32x32x16_bf16 v[2:17], v[172:175], v[240:243], v[2:17]
	v_mfma_f32_32x32x16_bf16 v[2:17], v[214:217], v[244:247], v[2:17]
	v_mfma_f32_32x32x16_bf16 v[2:17], v[230:233], v[222:225], v[2:17]
	ds_read_b64_tr_b16 v[222:223], v200 offset:0x200
	ds_read_b64_tr_b16 v[224:225], v200 offset:0xa00
	ds_read_b64_tr_b16 v[236:237], v200 offset:0x1200
	ds_read_b64_tr_b16 v[238:239], v200 offset:0x1a00
	ds_read_b64_tr_b16 v[240:241], v200 offset:0x2200
	ds_read_b64_tr_b16 v[242:243], v200 offset:0x2a00
	ds_read_b64_tr_b16 v[244:245], v200 offset:0x3200
	ds_read_b64_tr_b16 v[246:247], v200 offset:0x3a00
	s_waitcnt lgkmcnt(0)
	s_nop 0
	v_mfma_f32_32x32x16_bf16 v[50:65], v[168:171], v[222:225], v[50:65]
	ds_read_b64_tr_b16 v[222:223], v200 offset:0x400
	ds_read_b64_tr_b16 v[224:225], v200 offset:0xc00
	v_mfma_f32_32x32x16_bf16 v[50:65], v[172:175], v[236:239], v[50:65]
	ds_read_b64_tr_b16 v[236:237], v200 offset:0x1400
	ds_read_b64_tr_b16 v[238:239], v200 offset:0x1c00
	v_mfma_f32_32x32x16_bf16 v[50:65], v[214:217], v[240:243], v[50:65]
	ds_read_b64_tr_b16 v[240:241], v200 offset:0x2400
	ds_read_b64_tr_b16 v[242:243], v200 offset:0x2c00
	v_mfma_f32_32x32x16_bf16 v[50:65], v[230:233], v[244:247], v[50:65]
	ds_read_b64_tr_b16 v[244:245], v200 offset:0x3400
	ds_read_b64_tr_b16 v[246:247], v200 offset:0x3c00
	s_waitcnt lgkmcnt(0)
	v_mfma_f32_32x32x16_bf16 v[34:49], v[168:171], v[222:225], v[34:49]
	ds_read_b64_tr_b16 v[222:223], v200 offset:0x600
	ds_read_b64_tr_b16 v[224:225], v200 offset:0xe00
	v_mfma_f32_32x32x16_bf16 v[34:49], v[172:175], v[236:239], v[34:49]
	ds_read_b64_tr_b16 v[236:237], v200 offset:0x1600
	ds_read_b64_tr_b16 v[238:239], v200 offset:0x1e00
	v_mfma_f32_32x32x16_bf16 v[34:49], v[214:217], v[240:243], v[34:49]
	ds_read_b64_tr_b16 v[240:241], v200 offset:0x2600
	ds_read_b64_tr_b16 v[242:243], v200 offset:0x2e00
	v_mfma_f32_32x32x16_bf16 v[34:49], v[230:233], v[244:247], v[34:49]
	ds_read_b64_tr_b16 v[244:245], v200 offset:0x3600
	ds_read_b64_tr_b16 v[246:247], v200 offset:0x3e00
	s_waitcnt lgkmcnt(0)
	v_mfma_f32_32x32x16_bf16 v[18:33], v[168:171], v[222:225], v[18:33]
	v_max_f32_e32 v168, v83, v83
	v_max_f32_e32 v169, v82, v82
	v_max_f32_e32 v168, v169, v168
	v_max3_f32 v168, v168, v84, v85
	v_max3_f32 v168, v168, v86, v87
	v_max3_f32 v168, v168, v88, v89
	v_max3_f32 v168, v168, v90, v91
	v_max3_f32 v168, v168, v92, v93
	v_max3_f32 v168, v168, v94, v95
	v_mfma_f32_32x32x16_bf16 v[18:33], v[172:175], v[236:239], v[18:33]
	v_max3_f32 v168, v168, v96, v97
	v_max3_f32 v168, v168, v66, v67
	v_max3_f32 v168, v168, v68, v69
	v_max3_f32 v168, v168, v70, v71
	v_max3_f32 v168, v168, v72, v73
	v_max3_f32 v168, v168, v74, v75
	v_max3_f32 v168, v168, v76, v77
	v_max3_f32 v168, v168, v78, v79
	v_mfma_f32_32x32x16_bf16 v[18:33], v[214:217], v[240:243], v[18:33]
	v_max3_f32 v168, v168, v80, v81
	v_mov_b32_e32 v169, v168
	s_nop 1
	v_permlane32_swap_b32_e32 v168, v169
	v_max_f32_e32 v169, v169, v169
	v_max_f32_e32 v168, v168, v168
	v_max_f32_e32 v168, v168, v169
	v_sub_f32_e32 v169, v168, v211
	v_cmp_ge_f32_e32 vcc, s11, v169
	v_max_f32_e32 v169, v211, v211
	v_max_f32_e32 v168, v169, v168
	v_mfma_f32_32x32x16_bf16 v[18:33], v[230:233], v[244:247], v[18:33]
	v_sub_f32_e32 v169, v211, v168
	v_mul_f32_e32 v169, 0x3dd53b94, v169
	v_exp_f32_e32 v169, v169
	s_cmp_eq_u64 vcc, exec
	s_cselect_b64 s[18:19], -1, 0
	v_cndmask_b32_e64 v172, v169, 1.0, s[18:19]
	v_cmp_gt_f32_e32 vcc, 1.0, v172
	s_cbranch_vccz .LBB0_1348
	s_and_saveexec_b64 s[4:5], s[0:1]
	ds_write_b32 v197, v172 offset:128
	s_or_b64 exec, exec, s[4:5]
	s_waitcnt lgkmcnt(0)
	v_add_u32_e32 v160, v196, v98
	ds_read_b128 v[148:151], v160 offset:224
	ds_read_b128 v[152:155], v160 offset:192
	ds_read_b128 v[156:159], v160 offset:160
	ds_read_b128 v[160:163], v160 offset:128
	v_mov_b32_e32 v228, 0xffffce00
	s_waitcnt lgkmcnt(3)
	v_pk_mul_f32 v[14:15], v[14:15], v[148:149]
	s_waitcnt lgkmcnt(2)
	v_pk_mul_f32 v[10:11], v[10:11], v[152:153]
	s_waitcnt lgkmcnt(1)
	v_pk_mul_f32 v[6:7], v[6:7], v[156:157]
	v_pk_mul_f32 v[16:17], v[16:17], v[150:151]
	v_pk_mul_f32 v[12:13], v[12:13], v[154:155]
	v_pk_mul_f32 v[8:9], v[8:9], v[158:159]
	s_waitcnt lgkmcnt(0)
	v_pk_mul_f32 v[4:5], v[4:5], v[162:163]
	v_pk_mul_f32 v[2:3], v[2:3], v[160:161]
	v_pk_mul_f32 v[62:63], v[62:63], v[148:149]
	v_pk_mul_f32 v[58:59], v[58:59], v[152:153]
	v_pk_mul_f32 v[54:55], v[54:55], v[156:157]
	v_pk_mul_f32 v[64:65], v[64:65], v[150:151]
	v_pk_mul_f32 v[60:61], v[60:61], v[154:155]
	v_pk_mul_f32 v[56:57], v[56:57], v[158:159]
	v_pk_mul_f32 v[52:53], v[52:53], v[162:163]
	v_pk_mul_f32 v[50:51], v[50:51], v[160:161]
	v_pk_mul_f32 v[46:47], v[46:47], v[148:149]
	v_pk_mul_f32 v[42:43], v[42:43], v[152:153]
	v_pk_mul_f32 v[38:39], v[38:39], v[156:157]
	v_pk_mul_f32 v[48:49], v[48:49], v[150:151]
	v_pk_mul_f32 v[44:45], v[44:45], v[154:155]
	v_pk_mul_f32 v[40:41], v[40:41], v[158:159]
	v_pk_mul_f32 v[36:37], v[36:37], v[162:163]
	v_pk_mul_f32 v[34:35], v[34:35], v[160:161]
	v_pk_mul_f32 v[30:31], v[30:31], v[148:149]
	v_pk_mul_f32 v[26:27], v[26:27], v[152:153]
	v_pk_mul_f32 v[22:23], v[22:23], v[156:157]
	v_pk_mul_f32 v[32:33], v[32:33], v[150:151]
	v_pk_mul_f32 v[28:29], v[28:29], v[154:155]
	v_pk_mul_f32 v[24:25], v[24:25], v[158:159]
	v_pk_mul_f32 v[20:21], v[20:21], v[162:163]
	v_pk_mul_f32 v[18:19], v[18:19], v[160:161]
	s_branch .LBB0_1349

.LBB0_1356:
	s_setprio 0
	v_readfirstlane_b32 s4, v0
	s_nop 0
	s_lshl_b32 s5, s4, 4
	s_lshl_b32 s5, s5, 1
	s_add_i32 m0, s5, 0x4000
	s_nop 0
	global_load_lds_dwordx4 v[206:207], off
	s_add_i32 m0, s5, 0x4380
	s_nop 0
	global_load_lds_dwordx4 v[206:207], off offset:128
	ds_read_b128 v[182:185], v203 offset:24576
	ds_read_b128 v[206:209], v203 offset:36864
	ds_read_b128 v[230:233], v204 offset:24576
	ds_read_b128 v[236:239], v204 offset:36864
	ds_read_b128 v[66:69], v201 offset:36864
	ds_read_b128 v[70:73], v201 offset:24576
	s_waitcnt lgkmcnt(0)
	v_mfma_f32_32x32x16_bf16 v[82:97], v[70:73], v[128:131], 0
	v_mfma_f32_32x32x16_bf16 v[82:97], v[182:185], v[124:127], v[82:97]
	v_mfma_f32_32x32x16_bf16 v[66:81], v[66:69], v[128:131], 0
	ds_read_b128 v[128:131], v202 offset:24576
	ds_read_b128 v[240:243], v202 offset:36864
	v_mfma_f32_32x32x16_bf16 v[82:97], v[230:233], v[120:123], v[82:97]
	v_mfma_f32_32x32x16_bf16 v[66:81], v[206:209], v[124:127], v[66:81]
	ds_read_b128 v[124:127], v201 offset:24704
	ds_read_b128 v[182:185], v201 offset:36992
	s_waitcnt lgkmcnt(3)
	v_mfma_f32_32x32x16_bf16 v[82:97], v[128:131], v[116:119], v[82:97]
	v_mfma_f32_32x32x16_bf16 v[66:81], v[236:239], v[120:123], v[66:81]
	ds_read_b128 v[120:123], v203 offset:24704
	ds_read_b128 v[206:209], v203 offset:36992
	s_waitcnt lgkmcnt(3)
	v_mfma_f32_32x32x16_bf16 v[82:97], v[124:127], v[112:115], v[82:97]
	v_mfma_f32_32x32x16_bf16 v[66:81], v[240:243], v[116:119], v[66:81]
	ds_read_b128 v[116:119], v204 offset:24704
	ds_read_b128 v[128:131], v204 offset:36992
	s_waitcnt lgkmcnt(3)
	v_mfma_f32_32x32x16_bf16 v[82:97], v[120:123], v[108:111], v[82:97]
	v_mfma_f32_32x32x16_bf16 v[66:81], v[182:185], v[112:115], v[66:81]
	ds_read_b128 v[112:115], v202 offset:24704
	ds_read_b128 v[124:127], v202 offset:36992
	s_waitcnt lgkmcnt(3)
	v_mfma_f32_32x32x16_bf16 v[82:97], v[116:119], v[104:107], v[82:97]
	v_mfma_f32_32x32x16_bf16 v[66:81], v[206:209], v[108:111], v[66:81]
	ds_read_b128 v[108:111], v201 offset:24832
	ds_read_b128 v[120:123], v201 offset:37120
	s_waitcnt lgkmcnt(3)
	v_mfma_f32_32x32x16_bf16 v[82:97], v[112:115], v[100:103], v[82:97]
	v_mfma_f32_32x32x16_bf16 v[66:81], v[128:131], v[104:107], v[66:81]
	ds_read_b128 v[104:107], v203 offset:24832
	ds_read_b128 v[116:119], v203 offset:37120
	s_waitcnt lgkmcnt(3)
	v_mfma_f32_32x32x16_bf16 v[82:97], v[108:111], v[144:147], v[82:97]
	v_mfma_f32_32x32x16_bf16 v[66:81], v[124:127], v[100:103], v[66:81]
	ds_read_b128 v[100:103], v204 offset:24832
	ds_read_b128 v[112:115], v204 offset:37120
	v_exp_f32_e32 v124, v148
	v_exp_f32_e32 v125, v149
	s_waitcnt lgkmcnt(3)
	v_mfma_f32_32x32x16_bf16 v[82:97], v[104:107], v[140:143], v[82:97]
	v_mfma_f32_32x32x16_bf16 v[66:81], v[120:123], v[144:147], v[66:81]
	ds_read_b128 v[108:111], v202 offset:24832
	ds_read_b128 v[120:123], v202 offset:37120
	s_waitcnt lgkmcnt(3)
	v_mfma_f32_32x32x16_bf16 v[82:97], v[100:103], v[136:139], v[82:97]
	v_add_f32_e32 v100, 0, v169
	v_add_f32_e32 v100, v191, v100
	v_add_f32_e32 v100, v170, v100
	v_add_f32_e32 v100, v192, v100
	v_add_f32_e32 v100, v190, v100
	v_add_f32_e32 v100, v193, v100
	v_add_f32_e32 v100, v171, v100
	v_mfma_f32_32x32x16_bf16 v[66:81], v[116:119], v[140:143], v[66:81]
	v_add_f32_e32 v100, v189, v100
	v_add_f32_e32 v100, v173, v100
	v_add_f32_e32 v100, v175, v100
	v_add_f32_e32 v100, v174, v100
	v_add_f32_e32 v100, v188, v100
	v_add_f32_e32 v100, v164, v100
	v_add_f32_e32 v100, v166, v100
	s_waitcnt lgkmcnt(1)
	v_mfma_f32_32x32x16_bf16 v[82:97], v[108:111], v[132:135], v[82:97]
	v_exp_f32_e32 v110, v162
	v_exp_f32_e32 v111, v163
	v_add_f32_e32 v100, v165, v100
	v_add_f32_e32 v100, v167, v100
	v_add_f32_e32 v100, v110, v100
	v_add_f32_e32 v100, v111, v100
	v_exp_f32_e32 v116, v152
	v_mfma_f32_32x32x16_bf16 v[66:81], v[112:115], v[136:139], v[66:81]
	v_exp_f32_e32 v112, v160
	v_exp_f32_e32 v113, v161
	v_exp_f32_e32 v114, v156
	v_exp_f32_e32 v115, v157
	v_add_f32_e32 v100, v112, v100
	v_exp_f32_e32 v117, v153
	v_add_f32_e32 v100, v113, v100
	v_exp_f32_e32 v118, v150
	v_add_f32_e32 v100, v114, v100
	v_exp_f32_e32 v119, v151
	v_add_f32_e32 v100, v115, v100
	s_waitcnt lgkmcnt(0)
	v_mfma_f32_32x32x16_bf16 v[66:81], v[120:123], v[132:135], v[66:81]
	v_exp_f32_e32 v120, v158
	v_add_f32_e32 v100, v116, v100
	v_exp_f32_e32 v121, v159
	v_add_f32_e32 v100, v117, v100
	v_exp_f32_e32 v122, v154
	v_add_f32_e32 v100, v118, v100
	v_exp_f32_e32 v123, v155
	v_add_f32_e32 v100, v119, v100
	v_add_f32_e32 v100, v120, v100
	v_add_f32_e32 v100, v121, v100
	v_add_f32_e32 v100, v122, v100
	v_add_f32_e32 v100, v123, v100
	v_add_f32_e32 v100, v124, v100
	v_add_f32_e32 v104, v125, v100
	v_mov_b32_e32 v105, v104
	v_cvt_pk_bf16_f32 v100, v169, v191
	v_cvt_pk_bf16_f32 v101, v170, v192
	v_cvt_pk_bf16_f32 v102, v190, v193
	v_cvt_pk_bf16_f32 v103, v171, v189
	s_nop 1
	v_permlane32_swap_b32_e32 v104, v105
	v_permlane32_swap_b32_e32 v100, v102
	v_permlane32_swap_b32_e32 v101, v103
	v_cvt_pk_bf16_f32 v106, v173, v175
	v_cvt_pk_bf16_f32 v107, v174, v188
	v_cvt_pk_bf16_f32 v108, v164, v166
	v_cvt_pk_bf16_f32 v109, v165, v167
	v_cvt_pk_bf16_f32 v110, v110, v111
	v_cvt_pk_bf16_f32 v111, v112, v113
	v_cvt_pk_bf16_f32 v112, v114, v115
	v_cvt_pk_bf16_f32 v113, v116, v117
	v_cvt_pk_bf16_f32 v114, v118, v119
	v_cvt_pk_bf16_f32 v115, v120, v121
	v_cvt_pk_bf16_f32 v116, v122, v123
	v_cvt_pk_bf16_f32 v117, v124, v125
	s_nop 0
	v_permlane32_swap_b32_e32 v106, v108
	v_permlane32_swap_b32_e32 v107, v109
	v_permlane32_swap_b32_e32 v110, v112
	v_permlane32_swap_b32_e32 v111, v113
	v_permlane32_swap_b32_e32 v114, v116
	v_permlane32_swap_b32_e32 v115, v117
	ds_read_b64_tr_b16 v[118:119], v200 offset:0
	ds_read_b64_tr_b16 v[120:121], v200 offset:0x800
	ds_read_b64_tr_b16 v[122:123], v200 offset:0x1000
	ds_read_b64_tr_b16 v[124:125], v200 offset:0x1800
	ds_read_b64_tr_b16 v[126:127], v200 offset:0x2000
	ds_read_b64_tr_b16 v[128:129], v200 offset:0x2800
	ds_read_b64_tr_b16 v[130:131], v200 offset:0x3000
	ds_read_b64_tr_b16 v[132:133], v200 offset:0x3800
	s_waitcnt lgkmcnt(0)
	s_nop 0
	v_mfma_f32_32x32x16_bf16 v[2:17], v[100:103], v[118:121], v[2:17]
	ds_read_b64_tr_b16 v[118:119], v200 offset:0x200
	ds_read_b64_tr_b16 v[120:121], v200 offset:0xa00
	v_mfma_f32_32x32x16_bf16 v[2:17], v[106:109], v[122:125], v[2:17]
	ds_read_b64_tr_b16 v[122:123], v200 offset:0x1200
	ds_read_b64_tr_b16 v[124:125], v200 offset:0x1a00
	v_mfma_f32_32x32x16_bf16 v[2:17], v[110:113], v[126:129], v[2:17]
	ds_read_b64_tr_b16 v[126:127], v200 offset:0x2200
	ds_read_b64_tr_b16 v[128:129], v200 offset:0x2a00
	v_mfma_f32_32x32x16_bf16 v[2:17], v[114:117], v[130:133], v[2:17]
	ds_read_b64_tr_b16 v[130:131], v200 offset:0x3200
	ds_read_b64_tr_b16 v[132:133], v200 offset:0x3a00
	s_waitcnt lgkmcnt(0)
	v_mfma_f32_32x32x16_bf16 v[50:65], v[100:103], v[118:121], v[50:65]
	ds_read_b64_tr_b16 v[118:119], v200 offset:0x400
	ds_read_b64_tr_b16 v[120:121], v200 offset:0xc00
	v_mfma_f32_32x32x16_bf16 v[50:65], v[106:109], v[122:125], v[50:65]
	ds_read_b64_tr_b16 v[122:123], v200 offset:0x1400
	ds_read_b64_tr_b16 v[124:125], v200 offset:0x1c00
	v_mfma_f32_32x32x16_bf16 v[50:65], v[110:113], v[126:129], v[50:65]
	ds_read_b64_tr_b16 v[126:127], v200 offset:0x2400
	ds_read_b64_tr_b16 v[128:129], v200 offset:0x2c00
	v_mfma_f32_32x32x16_bf16 v[50:65], v[114:117], v[130:133], v[50:65]
	ds_read_b64_tr_b16 v[130:131], v200 offset:0x3400
	ds_read_b64_tr_b16 v[132:133], v200 offset:0x3c00
	s_waitcnt lgkmcnt(0)
	v_mfma_f32_32x32x16_bf16 v[34:49], v[100:103], v[118:121], v[34:49]
	ds_read_b64_tr_b16 v[118:119], v200 offset:0x600
	ds_read_b64_tr_b16 v[120:121], v200 offset:0xe00
	v_mfma_f32_32x32x16_bf16 v[34:49], v[106:109], v[122:125], v[34:49]
	ds_read_b64_tr_b16 v[122:123], v200 offset:0x1600
	ds_read_b64_tr_b16 v[124:125], v200 offset:0x1e00
	v_mfma_f32_32x32x16_bf16 v[34:49], v[110:113], v[126:129], v[34:49]
	ds_read_b64_tr_b16 v[126:127], v200 offset:0x2600
	ds_read_b64_tr_b16 v[128:129], v200 offset:0x2e00
	v_mfma_f32_32x32x16_bf16 v[34:49], v[114:117], v[130:133], v[34:49]
	ds_read_b64_tr_b16 v[130:131], v200 offset:0x3600
	ds_read_b64_tr_b16 v[132:133], v200 offset:0x3e00
	s_waitcnt lgkmcnt(0)
	v_mfma_f32_32x32x16_bf16 v[18:33], v[100:103], v[118:121], v[18:33]
	v_max_f32_e32 v100, v83, v83
	v_max_f32_e32 v101, v82, v82
	v_max_f32_e32 v100, v101, v100
	v_max3_f32 v100, v100, v84, v85
	v_max3_f32 v100, v100, v86, v87
	v_max3_f32 v100, v100, v88, v89
	v_max3_f32 v100, v100, v90, v91
	v_max3_f32 v100, v100, v92, v93
	v_max3_f32 v100, v100, v94, v95
	v_mfma_f32_32x32x16_bf16 v[18:33], v[106:109], v[122:125], v[18:33]
	v_max3_f32 v100, v100, v96, v97
	v_max3_f32 v100, v100, v66, v67
	v_max3_f32 v100, v100, v68, v69
	v_max3_f32 v100, v100, v70, v71
	v_max3_f32 v100, v100, v72, v73
	v_max3_f32 v100, v100, v74, v75
	v_max3_f32 v100, v100, v76, v77
	v_max3_f32 v100, v100, v78, v79
	v_mfma_f32_32x32x16_bf16 v[18:33], v[110:113], v[126:129], v[18:33]
	v_max3_f32 v100, v100, v80, v81
	v_mov_b32_e32 v101, v100
	s_nop 1
	v_permlane32_swap_b32_e32 v100, v101
	v_max_f32_e32 v101, v101, v101
	v_max_f32_e32 v100, v100, v100
	v_max_f32_e32 v100, v100, v101
	v_sub_f32_e32 v101, v100, v211
	v_cmp_ge_f32_e32 vcc, s11, v101
	v_max_f32_e32 v101, v211, v211
	v_max_f32_e32 v100, v101, v100
	v_mfma_f32_32x32x16_bf16 v[18:33], v[114:117], v[130:133], v[18:33]
	v_sub_f32_e32 v101, v211, v100
	v_mul_f32_e32 v101, 0x3dd53b94, v101
	v_exp_f32_e32 v101, v101
	s_cmp_eq_u64 vcc, exec
	s_cselect_b64 s[18:19], -1, 0
	v_mov_b32_e32 v229, v228
	v_cndmask_b32_e64 v102, v101, 1.0, s[18:19]
	v_cmp_gt_f32_e32 vcc, 1.0, v102
	s_waitcnt vmcnt(0)
	s_barrier
	s_cbranch_vccz .LBB0_1360
	s_and_saveexec_b64 s[4:5], s[0:1]
	ds_write_b32 v197, v102 offset:128
	s_or_b64 exec, exec, s[4:5]
	s_waitcnt lgkmcnt(0)
	v_add_u32_e32 v101, v196, v98
	ds_read_b128 v[106:109], v101 offset:224
	ds_read_b128 v[110:113], v101 offset:192
	ds_read_b128 v[114:117], v101 offset:160
	ds_read_b128 v[118:121], v101 offset:128
	s_waitcnt lgkmcnt(3)
	v_pk_mul_f32 v[14:15], v[14:15], v[106:107]
	s_waitcnt lgkmcnt(2)
	v_pk_mul_f32 v[10:11], v[10:11], v[110:111]
	s_waitcnt lgkmcnt(1)
	v_pk_mul_f32 v[6:7], v[6:7], v[114:115]
	v_pk_mul_f32 v[16:17], v[16:17], v[108:109]
	v_pk_mul_f32 v[12:13], v[12:13], v[112:113]
	v_pk_mul_f32 v[8:9], v[8:9], v[116:117]
	s_waitcnt lgkmcnt(0)
	v_pk_mul_f32 v[4:5], v[4:5], v[120:121]
	v_pk_mul_f32 v[2:3], v[2:3], v[118:119]
	v_pk_mul_f32 v[62:63], v[62:63], v[106:107]
	v_pk_mul_f32 v[58:59], v[58:59], v[110:111]
	v_pk_mul_f32 v[54:55], v[54:55], v[114:115]
	v_pk_mul_f32 v[64:65], v[64:65], v[108:109]
	v_pk_mul_f32 v[60:61], v[60:61], v[112:113]
	v_pk_mul_f32 v[56:57], v[56:57], v[116:117]
	v_pk_mul_f32 v[52:53], v[52:53], v[120:121]
	v_pk_mul_f32 v[50:51], v[50:51], v[118:119]
	v_pk_mul_f32 v[46:47], v[46:47], v[106:107]
	v_pk_mul_f32 v[42:43], v[42:43], v[110:111]
	v_pk_mul_f32 v[38:39], v[38:39], v[114:115]
	v_pk_mul_f32 v[48:49], v[48:49], v[108:109]
	v_pk_mul_f32 v[44:45], v[44:45], v[112:113]
	v_pk_mul_f32 v[40:41], v[40:41], v[116:117]
	v_pk_mul_f32 v[36:37], v[36:37], v[120:121]
	v_pk_mul_f32 v[34:35], v[34:35], v[118:119]
	v_pk_mul_f32 v[30:31], v[30:31], v[106:107]
	v_pk_mul_f32 v[26:27], v[26:27], v[110:111]
	v_pk_mul_f32 v[22:23], v[22:23], v[114:115]
	v_pk_mul_f32 v[32:33], v[32:33], v[108:109]
	v_pk_mul_f32 v[28:29], v[28:29], v[112:113]
	v_pk_mul_f32 v[24:25], v[24:25], v[116:117]
	v_pk_mul_f32 v[20:21], v[20:21], v[120:121]
	v_pk_mul_f32 v[18:19], v[18:19], v[118:119]
